# rebalanced LDS-DMA issue in the four fp8 GEMM loops: A stages in odd load segments, B stages in even (4 per segment), vmcnt(6) at even waits
# speedup vs baseline: 1.0053x; 1.0053x over previous
.LBB0_200:
	s_add_u32 s72, s42, 0xfff80000
	s_addc_u32 s73, s43, -1
	v_lshl_add_u64 v[246:247], s[72:73], 0, v[160:161]
	s_mov_b32 m0, s57
	s_nop 0
	global_load_lds_dwordx4 v[246:247], off
	v_lshl_add_u64 v[246:247], s[72:73], 0, v[164:165]
	s_mov_b32 m0, s58
	s_nop 0
	global_load_lds_dwordx4 v[246:247], off
	ds_read_b128 v[16:19], v186
	ds_read_b128 v[20:23], v187
	ds_read_b128 v[24:27], v188
	ds_read_b128 v[28:31], v189
	ds_read_b128 v[0:3], v190
	ds_read_b128 v[4:7], v191
	ds_read_b128 v[8:11], v192
	ds_read_b128 v[12:15], v193
	s_add_u32 s44, s42, 0xfff80080
	s_addc_u32 s45, s43, -1
	s_cmp_eq_u32 s68, 28
	s_cselect_b32 s47, s31, s45
	s_cselect_b32 s46, s35, s44
	s_cselect_b32 s45, s29, s67
	s_cselect_b32 s44, s39, s66
	v_lshl_add_u64 v[246:247], s[42:43], 0, v[172:173]
	s_add_i32 m0, s27, 0xc000
	ds_read_b128 v[178:181], v218
	ds_read_b128 v[182:185], v218 offset:1024
	ds_read_b128 v[222:225], v218 offset:2048
	ds_read_b128 v[226:229], v218 offset:3072
	ds_read_b128 v[230:233], v218 offset:4096
	ds_read_b128 v[234:237], v218 offset:5120
	ds_read_b128 v[238:241], v218 offset:6144
	ds_read_b128 v[242:245], v218 offset:7168
	global_load_lds_dwordx4 v[246:247], off
	v_lshl_add_u64 v[246:247], s[42:43], 0, v[174:175]
	s_add_i32 m0, s27, 0xe000
	s_nop 0
	global_load_lds_dwordx4 v[246:247], off
	s_waitcnt vmcnt(8)
	s_waitcnt lgkmcnt(0)
	s_barrier
	s_setprio 1
	s_waitcnt lgkmcnt(0)
	v_mfma_f32_16x16x128_f8f6f4 v[156:159], v[16:23], v[178:185], v[156:159]
	v_mfma_f32_16x16x128_f8f6f4 v[152:155], v[24:31], v[178:185], v[152:155]
	v_mfma_f32_16x16x128_f8f6f4 v[148:151], v[16:23], v[222:229], v[148:151]
	v_mfma_f32_16x16x128_f8f6f4 v[144:147], v[24:31], v[222:229], v[144:147]
	v_mfma_f32_16x16x128_f8f6f4 v[140:143], v[16:23], v[230:237], v[140:143]
	v_mfma_f32_16x16x128_f8f6f4 v[136:139], v[24:31], v[230:237], v[136:139]
	v_mfma_f32_16x16x128_f8f6f4 v[132:135], v[16:23], v[238:245], v[132:135]
	v_mfma_f32_16x16x128_f8f6f4 v[128:131], v[24:31], v[238:245], v[128:131]
	s_setprio 0
	s_setprio 1
	v_mfma_f32_16x16x128_f8f6f4 v[124:127], v[0:7], v[178:185], v[124:127]
	v_mfma_f32_16x16x128_f8f6f4 v[120:123], v[8:15], v[178:185], v[120:123]
	v_mfma_f32_16x16x128_f8f6f4 v[116:119], v[0:7], v[222:229], v[116:119]
	v_mfma_f32_16x16x128_f8f6f4 v[112:115], v[8:15], v[222:229], v[112:115]
	v_mfma_f32_16x16x128_f8f6f4 v[108:111], v[0:7], v[230:237], v[108:111]
	v_mfma_f32_16x16x128_f8f6f4 v[104:107], v[8:15], v[230:237], v[104:107]
	v_mfma_f32_16x16x128_f8f6f4 v[100:103], v[0:7], v[238:245], v[100:103]
	v_mfma_f32_16x16x128_f8f6f4 v[96:99], v[8:15], v[238:245], v[96:99]
	s_setprio 0
	s_barrier
	s_mov_b32 m0, s33
	v_lshl_add_u64 v[178:179], s[44:45], 0, v[162:163]
	s_add_u32 s70, s44, 0x80000
	ds_read_b128 v[222:225], v218 offset:16384
	ds_read_b128 v[226:229], v218 offset:17408
	ds_read_b128 v[230:233], v218 offset:18432
	ds_read_b128 v[234:237], v218 offset:19456
	ds_read_b128 v[238:241], v218 offset:20480
	ds_read_b128 v[242:245], v218 offset:21504
	ds_read_b128 v[246:249], v218 offset:22528
	ds_read_b128 v[250:253], v218 offset:23552
	global_load_lds_dwordx4 v[178:179], off
	v_lshl_add_u64 v[180:181], s[44:45], 0, v[166:167]
	s_mov_b32 m0, s48
	s_addc_u32 s71, s45, 0
	global_load_lds_dwordx4 v[180:181], off
	v_lshl_add_u64 v[182:183], s[70:71], 0, v[162:163]
	s_mov_b32 m0, s49
	global_load_lds_dwordx4 v[182:183], off
	v_lshl_add_u64 v[182:183], s[70:71], 0, v[166:167]
	s_mov_b32 m0, s50
	s_nop 0
	global_load_lds_dwordx4 v[182:183], off
	s_waitcnt vmcnt(6)
	s_waitcnt lgkmcnt(0)
	s_barrier
	s_setprio 1
	s_waitcnt lgkmcnt(0)
	v_mfma_f32_16x16x128_f8f6f4 v[92:95], v[16:23], v[222:229], v[92:95]
	v_mfma_f32_16x16x128_f8f6f4 v[88:91], v[24:31], v[222:229], v[88:91]
	v_mfma_f32_16x16x128_f8f6f4 v[84:87], v[16:23], v[230:237], v[84:87]
	v_mfma_f32_16x16x128_f8f6f4 v[80:83], v[24:31], v[230:237], v[80:83]
	v_mfma_f32_16x16x128_f8f6f4 v[76:79], v[16:23], v[238:245], v[76:79]
	v_mfma_f32_16x16x128_f8f6f4 v[72:75], v[24:31], v[238:245], v[72:75]
	v_mfma_f32_16x16x128_f8f6f4 v[68:71], v[16:23], v[246:253], v[68:71]
	v_mfma_f32_16x16x128_f8f6f4 v[64:67], v[24:31], v[246:253], v[64:67]
	s_setprio 0
	s_setprio 1
	v_mfma_f32_16x16x128_f8f6f4 v[60:63], v[0:7], v[222:229], v[60:63]
	v_mfma_f32_16x16x128_f8f6f4 v[56:59], v[8:15], v[222:229], v[56:59]
	v_mfma_f32_16x16x128_f8f6f4 v[52:55], v[0:7], v[230:237], v[52:55]
	v_mfma_f32_16x16x128_f8f6f4 v[48:51], v[8:15], v[230:237], v[48:51]
	v_mfma_f32_16x16x128_f8f6f4 v[44:47], v[0:7], v[238:245], v[44:47]
	v_mfma_f32_16x16x128_f8f6f4 v[40:43], v[8:15], v[238:245], v[40:43]
	v_mfma_f32_16x16x128_f8f6f4 v[36:39], v[0:7], v[246:253], v[36:39]
	v_mfma_f32_16x16x128_f8f6f4 v[32:35], v[8:15], v[246:253], v[32:35]
	s_setprio 0
	s_barrier
	v_lshl_add_u64 v[176:177], s[46:47], 0, v[160:161]
	s_mov_b32 m0, s27
	s_nop 0
	global_load_lds_dwordx4 v[176:177], off
	v_lshl_add_u64 v[176:177], s[46:47], 0, v[164:165]
	s_mov_b32 m0, s51
	s_nop 0
	global_load_lds_dwordx4 v[176:177], off
	ds_read_b128 v[0:3], v194
	ds_read_b128 v[4:7], v195
	ds_read_b128 v[8:11], v196
	ds_read_b128 v[12:15], v197
	ds_read_b128 v[16:19], v198
	ds_read_b128 v[20:23], v199
	ds_read_b128 v[24:27], v200
	ds_read_b128 v[28:31], v201
	s_add_u32 s46, s46, 0x80000
	s_addc_u32 s47, s47, 0
	s_mov_b32 m0, s52
	v_lshl_add_u64 v[176:177], s[46:47], 0, v[160:161]
	ds_read_b128 v[222:225], v218 offset:32768
	ds_read_b128 v[226:229], v218 offset:33792
	ds_read_b128 v[230:233], v218 offset:34816
	ds_read_b128 v[234:237], v218 offset:35840
	ds_read_b128 v[238:241], v218 offset:36864
	ds_read_b128 v[242:245], v218 offset:37888
	ds_read_b128 v[246:249], v218 offset:38912
	ds_read_b128 v[250:253], v218 offset:39936
	global_load_lds_dwordx4 v[176:177], off
	v_lshl_add_u64 v[176:177], s[46:47], 0, v[164:165]
	s_mov_b32 m0, s53
	s_nop 0
	global_load_lds_dwordx4 v[176:177], off
	s_waitcnt vmcnt(8)
	s_waitcnt lgkmcnt(0)
	s_barrier
	s_setprio 1
	s_waitcnt lgkmcnt(0)
	v_mfma_f32_16x16x128_f8f6f4 v[156:159], v[0:7], v[222:229], v[156:159]
	v_mfma_f32_16x16x128_f8f6f4 v[152:155], v[8:15], v[222:229], v[152:155]
	v_mfma_f32_16x16x128_f8f6f4 v[148:151], v[0:7], v[230:237], v[148:151]
	v_mfma_f32_16x16x128_f8f6f4 v[144:147], v[8:15], v[230:237], v[144:147]
	v_mfma_f32_16x16x128_f8f6f4 v[140:143], v[0:7], v[238:245], v[140:143]
	v_mfma_f32_16x16x128_f8f6f4 v[136:139], v[8:15], v[238:245], v[136:139]
	v_mfma_f32_16x16x128_f8f6f4 v[132:135], v[0:7], v[246:253], v[132:135]
	v_mfma_f32_16x16x128_f8f6f4 v[128:131], v[8:15], v[246:253], v[128:131]
	s_setprio 0
	s_setprio 1
	v_mfma_f32_16x16x128_f8f6f4 v[124:127], v[16:23], v[222:229], v[124:127]
	v_mfma_f32_16x16x128_f8f6f4 v[120:123], v[24:31], v[222:229], v[120:123]
	v_mfma_f32_16x16x128_f8f6f4 v[116:119], v[16:23], v[230:237], v[116:119]
	v_mfma_f32_16x16x128_f8f6f4 v[112:115], v[24:31], v[230:237], v[112:115]
	v_mfma_f32_16x16x128_f8f6f4 v[108:111], v[16:23], v[238:245], v[108:111]
	v_mfma_f32_16x16x128_f8f6f4 v[104:107], v[24:31], v[238:245], v[104:107]
	v_mfma_f32_16x16x128_f8f6f4 v[100:103], v[16:23], v[246:253], v[100:103]
	v_mfma_f32_16x16x128_f8f6f4 v[96:99], v[24:31], v[246:253], v[96:99]
	s_setprio 0
	s_barrier
	s_mov_b32 m0, s55
	v_lshl_add_u64 v[176:177], v[178:179], 0, s[20:21]
	s_add_u32 s44, s44, 0x80080
	ds_read_b128 v[222:225], v218 offset:49152
	ds_read_b128 v[226:229], v218 offset:50176
	ds_read_b128 v[230:233], v218 offset:51200
	ds_read_b128 v[234:237], v218 offset:52224
	ds_read_b128 v[238:241], v218 offset:53248
	ds_read_b128 v[242:245], v218 offset:54272
	ds_read_b128 v[246:249], v218 offset:55296
	ds_read_b128 v[250:253], v218 offset:56320
	global_load_lds_dwordx4 v[176:177], off
	v_lshl_add_u64 v[176:177], v[180:181], 0, s[20:21]
	s_mov_b32 m0, s56
	s_addc_u32 s45, s45, 0
	global_load_lds_dwordx4 v[176:177], off
	v_lshl_add_u64 v[176:177], s[44:45], 0, v[162:163]
	s_mov_b32 m0, s59
	s_nop 0
	global_load_lds_dwordx4 v[176:177], off
	v_lshl_add_u64 v[176:177], s[44:45], 0, v[166:167]
	s_mov_b32 m0, s60
	s_nop 0
	global_load_lds_dwordx4 v[176:177], off
	s_waitcnt vmcnt(6)
	s_waitcnt lgkmcnt(0)
	s_barrier
	s_setprio 1
	s_waitcnt lgkmcnt(0)
	v_mfma_f32_16x16x128_f8f6f4 v[92:95], v[0:7], v[222:229], v[92:95]
	v_mfma_f32_16x16x128_f8f6f4 v[88:91], v[8:15], v[222:229], v[88:91]
	v_mfma_f32_16x16x128_f8f6f4 v[84:87], v[0:7], v[230:237], v[84:87]
	v_mfma_f32_16x16x128_f8f6f4 v[80:83], v[8:15], v[230:237], v[80:83]
	v_mfma_f32_16x16x128_f8f6f4 v[76:79], v[0:7], v[238:245], v[76:79]
	v_mfma_f32_16x16x128_f8f6f4 v[72:75], v[8:15], v[238:245], v[72:75]
	v_mfma_f32_16x16x128_f8f6f4 v[68:71], v[0:7], v[246:253], v[68:71]
	v_mfma_f32_16x16x128_f8f6f4 v[64:67], v[8:15], v[246:253], v[64:67]
	s_setprio 0
	s_setprio 1
	v_mfma_f32_16x16x128_f8f6f4 v[60:63], v[16:23], v[222:229], v[60:63]
	v_mfma_f32_16x16x128_f8f6f4 v[56:59], v[24:31], v[222:229], v[56:59]
	v_mfma_f32_16x16x128_f8f6f4 v[52:55], v[16:23], v[230:237], v[52:55]
	v_mfma_f32_16x16x128_f8f6f4 v[48:51], v[24:31], v[230:237], v[48:51]
	v_mfma_f32_16x16x128_f8f6f4 v[44:47], v[16:23], v[238:245], v[44:47]
	v_mfma_f32_16x16x128_f8f6f4 v[40:43], v[24:31], v[238:245], v[40:43]
	v_mfma_f32_16x16x128_f8f6f4 v[36:39], v[16:23], v[246:253], v[36:39]
	v_mfma_f32_16x16x128_f8f6f4 v[32:35], v[24:31], v[246:253], v[32:35]
	s_setprio 0
	s_barrier
	s_add_i32 s68, s68, 2
	s_add_u32 s42, s42, 0x100
	s_addc_u32 s43, s43, 0
	s_add_u32 s66, s66, 0x100
	s_addc_u32 s67, s67, 0
	s_cmp_gt_u32 s68, 29
	s_cbranch_scc0 .LBB0_200
	s_nop 15
	s_nop 15
	s_and_b64 vcc, exec, s[22:23]
	s_cbranch_vccz .LBB0_203
	s_barrier

.LBB0_562:
	s_add_u32 s72, s30, 0xfff80000
	s_addc_u32 s73, s31, -1
	v_lshl_add_u64 v[224:225], s[72:73], 0, v[160:161]
	s_mov_b32 m0, s49
	s_nop 0
	global_load_lds_dwordx4 v[224:225], off
	v_lshl_add_u64 v[224:225], s[72:73], 0, v[162:163]
	s_mov_b32 m0, s50
	s_nop 0
	global_load_lds_dwordx4 v[224:225], off
	ds_read_b128 v[16:19], v181
	ds_read_b128 v[20:23], v182
	ds_read_b128 v[24:27], v183
	ds_read_b128 v[28:31], v184
	ds_read_b128 v[0:3], v185
	ds_read_b128 v[4:7], v186
	ds_read_b128 v[8:11], v187
	ds_read_b128 v[12:15], v188
	s_add_u32 s34, s30, 0xfff80080
	s_addc_u32 s35, s31, -1
	s_cmp_eq_u32 s59, 28
	s_cselect_b32 s37, s23, s35
	s_cselect_b32 s36, s55, s34
	s_cselect_b32 s35, s21, s58
	s_cselect_b32 s34, s56, s57
	v_lshl_add_u64 v[224:225], s[30:31], 0, v[164:165]
	s_add_i32 m0, s29, 0xc000
	ds_read_b128 v[172:175], v198
	ds_read_b128 v[176:179], v198 offset:1024
	ds_read_b128 v[200:203], v198 offset:2048
	ds_read_b128 v[204:207], v198 offset:3072
	ds_read_b128 v[208:211], v198 offset:4096
	ds_read_b128 v[212:215], v198 offset:5120
	ds_read_b128 v[216:219], v198 offset:6144
	ds_read_b128 v[220:223], v198 offset:7168
	global_load_lds_dwordx4 v[224:225], off
	v_lshl_add_u64 v[224:225], s[30:31], 0, v[166:167]
	s_add_i32 m0, s29, 0xe000
	s_nop 0
	global_load_lds_dwordx4 v[224:225], off
	s_waitcnt vmcnt(8)
	s_waitcnt lgkmcnt(0)
	s_barrier
	s_setprio 1
	s_waitcnt lgkmcnt(0)
	v_mfma_f32_16x16x128_f8f6f4 v[156:159], v[16:23], v[172:179], v[156:159]
	v_mfma_f32_16x16x128_f8f6f4 v[152:155], v[24:31], v[172:179], v[152:155]
	v_mfma_f32_16x16x128_f8f6f4 v[148:151], v[16:23], v[200:207], v[148:151]
	v_mfma_f32_16x16x128_f8f6f4 v[144:147], v[24:31], v[200:207], v[144:147]
	v_mfma_f32_16x16x128_f8f6f4 v[124:127], v[16:23], v[208:215], v[124:127]
	v_mfma_f32_16x16x128_f8f6f4 v[120:123], v[24:31], v[208:215], v[120:123]
	v_mfma_f32_16x16x128_f8f6f4 v[116:119], v[16:23], v[216:223], v[116:119]
	v_mfma_f32_16x16x128_f8f6f4 v[112:115], v[24:31], v[216:223], v[112:115]
	s_setprio 0
	s_setprio 1
	v_mfma_f32_16x16x128_f8f6f4 v[140:143], v[0:7], v[172:179], v[140:143]
	v_mfma_f32_16x16x128_f8f6f4 v[136:139], v[8:15], v[172:179], v[136:139]
	v_mfma_f32_16x16x128_f8f6f4 v[132:135], v[0:7], v[200:207], v[132:135]
	v_mfma_f32_16x16x128_f8f6f4 v[128:131], v[8:15], v[200:207], v[128:131]
	v_mfma_f32_16x16x128_f8f6f4 v[108:111], v[0:7], v[208:215], v[108:111]
	v_mfma_f32_16x16x128_f8f6f4 v[104:107], v[8:15], v[208:215], v[104:107]
	v_mfma_f32_16x16x128_f8f6f4 v[100:103], v[0:7], v[216:223], v[100:103]
	v_mfma_f32_16x16x128_f8f6f4 v[96:99], v[8:15], v[216:223], v[96:99]
	s_setprio 0
	s_barrier
	s_mov_b32 m0, s33
	v_lshl_add_u64 v[172:173], s[34:35], 0, v[160:161]
	s_add_u32 s60, s34, 0x80000
	ds_read_b128 v[200:203], v198 offset:16384
	ds_read_b128 v[204:207], v198 offset:17408
	ds_read_b128 v[208:211], v198 offset:18432
	ds_read_b128 v[212:215], v198 offset:19456
	ds_read_b128 v[216:219], v198 offset:20480
	ds_read_b128 v[220:223], v198 offset:21504
	ds_read_b128 v[224:227], v198 offset:22528
	ds_read_b128 v[228:231], v198 offset:23552
	global_load_lds_dwordx4 v[172:173], off
	v_lshl_add_u64 v[174:175], s[34:35], 0, v[162:163]
	s_mov_b32 m0, s38
	s_addc_u32 s61, s35, 0
	global_load_lds_dwordx4 v[174:175], off
	v_lshl_add_u64 v[176:177], s[60:61], 0, v[160:161]
	s_mov_b32 m0, s39
	global_load_lds_dwordx4 v[176:177], off
	v_lshl_add_u64 v[176:177], s[60:61], 0, v[162:163]
	s_mov_b32 m0, s40
	s_nop 0
	global_load_lds_dwordx4 v[176:177], off
	s_waitcnt vmcnt(6)
	s_waitcnt lgkmcnt(0)
	s_barrier
	s_setprio 1
	s_waitcnt lgkmcnt(0)
	v_mfma_f32_16x16x128_f8f6f4 v[92:95], v[16:23], v[200:207], v[92:95]
	v_mfma_f32_16x16x128_f8f6f4 v[88:91], v[24:31], v[200:207], v[88:91]
	v_mfma_f32_16x16x128_f8f6f4 v[84:87], v[16:23], v[208:215], v[84:87]
	v_mfma_f32_16x16x128_f8f6f4 v[80:83], v[24:31], v[208:215], v[80:83]
	v_mfma_f32_16x16x128_f8f6f4 v[60:63], v[16:23], v[216:223], v[60:63]
	v_mfma_f32_16x16x128_f8f6f4 v[56:59], v[24:31], v[216:223], v[56:59]
	v_mfma_f32_16x16x128_f8f6f4 v[52:55], v[16:23], v[224:231], v[52:55]
	v_mfma_f32_16x16x128_f8f6f4 v[48:51], v[24:31], v[224:231], v[48:51]
	s_setprio 0
	s_setprio 1
	v_mfma_f32_16x16x128_f8f6f4 v[76:79], v[0:7], v[200:207], v[76:79]
	v_mfma_f32_16x16x128_f8f6f4 v[72:75], v[8:15], v[200:207], v[72:75]
	v_mfma_f32_16x16x128_f8f6f4 v[68:71], v[0:7], v[208:215], v[68:71]
	v_mfma_f32_16x16x128_f8f6f4 v[64:67], v[8:15], v[208:215], v[64:67]
	v_mfma_f32_16x16x128_f8f6f4 v[44:47], v[0:7], v[216:223], v[44:47]
	v_mfma_f32_16x16x128_f8f6f4 v[40:43], v[8:15], v[216:223], v[40:43]
	v_mfma_f32_16x16x128_f8f6f4 v[36:39], v[0:7], v[224:231], v[36:39]
	v_mfma_f32_16x16x128_f8f6f4 v[32:35], v[8:15], v[224:231], v[32:35]
	s_setprio 0
	s_barrier
	v_lshl_add_u64 v[232:233], s[36:37], 0, v[160:161]
	s_mov_b32 m0, s29
	s_nop 0
	global_load_lds_dwordx4 v[232:233], off
	v_lshl_add_u64 v[232:233], s[36:37], 0, v[162:163]
	s_mov_b32 m0, s41
	s_nop 0
	global_load_lds_dwordx4 v[232:233], off
	ds_read_b128 v[0:3], v189
	ds_read_b128 v[4:7], v190
	ds_read_b128 v[8:11], v191
	ds_read_b128 v[12:15], v192
	ds_read_b128 v[16:19], v193
	ds_read_b128 v[20:23], v194
	ds_read_b128 v[24:27], v195
	ds_read_b128 v[28:31], v196
	s_add_u32 s36, s36, 0x80000
	s_addc_u32 s37, s37, 0
	s_mov_b32 m0, s42
	v_lshl_add_u64 v[232:233], s[36:37], 0, v[160:161]
	ds_read_b128 v[200:203], v198 offset:32768
	ds_read_b128 v[204:207], v198 offset:33792
	ds_read_b128 v[208:211], v198 offset:34816
	ds_read_b128 v[212:215], v198 offset:35840
	ds_read_b128 v[216:219], v198 offset:36864
	ds_read_b128 v[220:223], v198 offset:37888
	ds_read_b128 v[224:227], v198 offset:38912
	ds_read_b128 v[228:231], v198 offset:39936
	global_load_lds_dwordx4 v[232:233], off
	v_lshl_add_u64 v[232:233], s[36:37], 0, v[162:163]
	s_mov_b32 m0, s43
	s_nop 0
	global_load_lds_dwordx4 v[232:233], off
	s_waitcnt vmcnt(8)
	s_waitcnt lgkmcnt(0)
	s_barrier
	s_setprio 1
	s_waitcnt lgkmcnt(0)
	v_mfma_f32_16x16x128_f8f6f4 v[156:159], v[0:7], v[200:207], v[156:159]
	v_mfma_f32_16x16x128_f8f6f4 v[152:155], v[8:15], v[200:207], v[152:155]
	v_mfma_f32_16x16x128_f8f6f4 v[148:151], v[0:7], v[208:215], v[148:151]
	v_mfma_f32_16x16x128_f8f6f4 v[144:147], v[8:15], v[208:215], v[144:147]
	v_mfma_f32_16x16x128_f8f6f4 v[124:127], v[0:7], v[216:223], v[124:127]
	v_mfma_f32_16x16x128_f8f6f4 v[120:123], v[8:15], v[216:223], v[120:123]
	v_mfma_f32_16x16x128_f8f6f4 v[116:119], v[0:7], v[224:231], v[116:119]
	v_mfma_f32_16x16x128_f8f6f4 v[112:115], v[8:15], v[224:231], v[112:115]
	s_setprio 0
	s_setprio 1
	v_mfma_f32_16x16x128_f8f6f4 v[140:143], v[16:23], v[200:207], v[140:143]
	v_mfma_f32_16x16x128_f8f6f4 v[136:139], v[24:31], v[200:207], v[136:139]
	v_mfma_f32_16x16x128_f8f6f4 v[132:135], v[16:23], v[208:215], v[132:135]
	v_mfma_f32_16x16x128_f8f6f4 v[128:131], v[24:31], v[208:215], v[128:131]
	v_mfma_f32_16x16x128_f8f6f4 v[108:111], v[16:23], v[216:223], v[108:111]
	v_mfma_f32_16x16x128_f8f6f4 v[104:107], v[24:31], v[216:223], v[104:107]
	v_mfma_f32_16x16x128_f8f6f4 v[100:103], v[16:23], v[224:231], v[100:103]
	v_mfma_f32_16x16x128_f8f6f4 v[96:99], v[24:31], v[224:231], v[96:99]
	s_setprio 0
	s_barrier
	s_mov_b32 m0, s47
	v_lshl_add_u64 v[172:173], v[172:173], 0, s[14:15]
	s_add_u32 s34, s34, 0x80080
	ds_read_b128 v[200:203], v198 offset:49152
	ds_read_b128 v[204:207], v198 offset:50176
	ds_read_b128 v[208:211], v198 offset:51200
	ds_read_b128 v[212:215], v198 offset:52224
	ds_read_b128 v[216:219], v198 offset:53248
	ds_read_b128 v[220:223], v198 offset:54272
	ds_read_b128 v[224:227], v198 offset:55296
	ds_read_b128 v[228:231], v198 offset:56320
	global_load_lds_dwordx4 v[172:173], off
	v_lshl_add_u64 v[172:173], v[174:175], 0, s[14:15]
	s_mov_b32 m0, s48
	s_addc_u32 s35, s35, 0
	global_load_lds_dwordx4 v[172:173], off
	v_lshl_add_u64 v[172:173], s[34:35], 0, v[160:161]
	s_mov_b32 m0, s51
	s_nop 0
	global_load_lds_dwordx4 v[172:173], off
	v_lshl_add_u64 v[172:173], s[34:35], 0, v[162:163]
	s_mov_b32 m0, s52
	s_nop 0
	global_load_lds_dwordx4 v[172:173], off
	s_waitcnt vmcnt(6)
	s_waitcnt lgkmcnt(0)
	s_barrier
	s_setprio 1
	s_waitcnt lgkmcnt(0)
	v_mfma_f32_16x16x128_f8f6f4 v[92:95], v[0:7], v[200:207], v[92:95]
	v_mfma_f32_16x16x128_f8f6f4 v[88:91], v[8:15], v[200:207], v[88:91]
	v_mfma_f32_16x16x128_f8f6f4 v[84:87], v[0:7], v[208:215], v[84:87]
	v_mfma_f32_16x16x128_f8f6f4 v[80:83], v[8:15], v[208:215], v[80:83]
	v_mfma_f32_16x16x128_f8f6f4 v[60:63], v[0:7], v[216:223], v[60:63]
	v_mfma_f32_16x16x128_f8f6f4 v[56:59], v[8:15], v[216:223], v[56:59]
	v_mfma_f32_16x16x128_f8f6f4 v[52:55], v[0:7], v[224:231], v[52:55]
	v_mfma_f32_16x16x128_f8f6f4 v[48:51], v[8:15], v[224:231], v[48:51]
	s_setprio 0
	s_setprio 1
	v_mfma_f32_16x16x128_f8f6f4 v[76:79], v[16:23], v[200:207], v[76:79]
	v_mfma_f32_16x16x128_f8f6f4 v[72:75], v[24:31], v[200:207], v[72:75]
	v_mfma_f32_16x16x128_f8f6f4 v[68:71], v[16:23], v[208:215], v[68:71]
	v_mfma_f32_16x16x128_f8f6f4 v[64:67], v[24:31], v[208:215], v[64:67]
	v_mfma_f32_16x16x128_f8f6f4 v[44:47], v[16:23], v[216:223], v[44:47]
	v_mfma_f32_16x16x128_f8f6f4 v[40:43], v[24:31], v[216:223], v[40:43]
	v_mfma_f32_16x16x128_f8f6f4 v[36:39], v[16:23], v[224:231], v[36:39]
	v_mfma_f32_16x16x128_f8f6f4 v[32:35], v[24:31], v[224:231], v[32:35]
	s_setprio 0
	s_barrier
	s_add_i32 s59, s59, 2
	s_add_u32 s30, s30, 0x100
	s_addc_u32 s31, s31, 0
	s_add_u32 s57, s57, 0x100
	s_addc_u32 s58, s58, 0
	s_cmp_gt_u32 s59, 29
	s_cbranch_scc0 .LBB0_562
	s_nop 15
	s_nop 15
	s_and_b64 vcc, exec, s[16:17]
	s_cbranch_vccz .LBB0_565
	s_barrier

.LBB0_940:
	s_add_u32 s72, s38, 0xfff80000
	s_addc_u32 s73, s39, -1
	v_lshl_add_u64 v[232:233], s[72:73], 0, v[160:161]
	s_mov_b32 m0, s53
	s_nop 0
	global_load_lds_dwordx4 v[232:233], off
	v_lshl_add_u64 v[232:233], s[72:73], 0, v[164:165]
	s_mov_b32 m0, s54
	s_nop 0
	global_load_lds_dwordx4 v[232:233], off
	ds_read_b128 v[16:19], v189
	ds_read_b128 v[20:23], v190
	ds_read_b128 v[24:27], v191
	ds_read_b128 v[28:31], v192
	ds_read_b128 v[0:3], v193
	ds_read_b128 v[4:7], v194
	ds_read_b128 v[8:11], v195
	ds_read_b128 v[12:15], v196
	s_add_u32 s40, s38, 0xfff80080
	s_addc_u32 s41, s39, -1
	s_cmp_eq_u32 s64, 28
	s_cselect_b32 s43, s27, s41
	s_cselect_b32 s42, s35, s40
	s_cselect_b32 s41, s25, s61
	s_cselect_b32 s40, s37, s60
	v_lshl_add_u64 v[232:233], s[38:39], 0, v[172:173]
	s_add_i32 m0, s33, 0xc000
	ds_read_b128 v[180:183], v205
	ds_read_b128 v[184:187], v205 offset:1024
	ds_read_b128 v[208:211], v205 offset:2048
	ds_read_b128 v[212:215], v205 offset:3072
	ds_read_b128 v[216:219], v205 offset:4096
	ds_read_b128 v[220:223], v205 offset:5120
	ds_read_b128 v[224:227], v205 offset:6144
	ds_read_b128 v[228:231], v205 offset:7168
	global_load_lds_dwordx4 v[232:233], off
	v_lshl_add_u64 v[232:233], s[38:39], 0, v[174:175]
	s_add_i32 m0, s33, 0xe000
	s_nop 0
	global_load_lds_dwordx4 v[232:233], off
	s_waitcnt vmcnt(8)
	s_waitcnt lgkmcnt(0)
	s_barrier
	s_setprio 1
	s_waitcnt lgkmcnt(0)
	v_mfma_f32_16x16x128_f8f6f4 v[156:159], v[16:23], v[180:187], v[156:159]
	v_mfma_f32_16x16x128_f8f6f4 v[152:155], v[24:31], v[180:187], v[152:155]
	v_mfma_f32_16x16x128_f8f6f4 v[140:143], v[16:23], v[208:215], v[140:143]
	v_mfma_f32_16x16x128_f8f6f4 v[136:139], v[24:31], v[208:215], v[136:139]
	v_mfma_f32_16x16x128_f8f6f4 v[124:127], v[16:23], v[216:223], v[124:127]
	v_mfma_f32_16x16x128_f8f6f4 v[120:123], v[24:31], v[216:223], v[120:123]
	v_mfma_f32_16x16x128_f8f6f4 v[108:111], v[16:23], v[224:231], v[108:111]
	v_mfma_f32_16x16x128_f8f6f4 v[104:107], v[24:31], v[224:231], v[104:107]
	s_setprio 0
	s_setprio 1
	v_mfma_f32_16x16x128_f8f6f4 v[148:151], v[0:7], v[180:187], v[148:151]
	v_mfma_f32_16x16x128_f8f6f4 v[144:147], v[8:15], v[180:187], v[144:147]
	v_mfma_f32_16x16x128_f8f6f4 v[132:135], v[0:7], v[208:215], v[132:135]
	v_mfma_f32_16x16x128_f8f6f4 v[128:131], v[8:15], v[208:215], v[128:131]
	v_mfma_f32_16x16x128_f8f6f4 v[116:119], v[0:7], v[216:223], v[116:119]
	v_mfma_f32_16x16x128_f8f6f4 v[112:115], v[8:15], v[216:223], v[112:115]
	v_mfma_f32_16x16x128_f8f6f4 v[100:103], v[0:7], v[224:231], v[100:103]
	v_mfma_f32_16x16x128_f8f6f4 v[96:99], v[8:15], v[224:231], v[96:99]
	s_setprio 0
	s_barrier
	s_mov_b32 m0, s44
	v_lshl_add_u64 v[180:181], s[40:41], 0, v[162:163]
	s_add_u32 s62, s40, 0x80000
	ds_read_b128 v[208:211], v205 offset:16384
	ds_read_b128 v[212:215], v205 offset:17408
	ds_read_b128 v[216:219], v205 offset:18432
	ds_read_b128 v[220:223], v205 offset:19456
	ds_read_b128 v[224:227], v205 offset:20480
	ds_read_b128 v[228:231], v205 offset:21504
	ds_read_b128 v[232:235], v205 offset:22528
	ds_read_b128 v[236:239], v205 offset:23552
	global_load_lds_dwordx4 v[180:181], off
	v_lshl_add_u64 v[182:183], s[40:41], 0, v[166:167]
	s_mov_b32 m0, s45
	s_addc_u32 s63, s41, 0
	global_load_lds_dwordx4 v[182:183], off
	v_lshl_add_u64 v[184:185], s[62:63], 0, v[162:163]
	s_mov_b32 m0, s46
	global_load_lds_dwordx4 v[184:185], off
	v_lshl_add_u64 v[184:185], s[62:63], 0, v[166:167]
	s_mov_b32 m0, s47
	s_nop 0
	global_load_lds_dwordx4 v[184:185], off
	s_waitcnt vmcnt(6)
	s_waitcnt lgkmcnt(0)
	s_barrier
	s_setprio 1
	s_waitcnt lgkmcnt(0)
	v_mfma_f32_16x16x128_f8f6f4 v[92:95], v[16:23], v[208:215], v[92:95]
	v_mfma_f32_16x16x128_f8f6f4 v[88:91], v[24:31], v[208:215], v[88:91]
	v_mfma_f32_16x16x128_f8f6f4 v[76:79], v[16:23], v[216:223], v[76:79]
	v_mfma_f32_16x16x128_f8f6f4 v[72:75], v[24:31], v[216:223], v[72:75]
	v_mfma_f32_16x16x128_f8f6f4 v[60:63], v[16:23], v[224:231], v[60:63]
	v_mfma_f32_16x16x128_f8f6f4 v[56:59], v[24:31], v[224:231], v[56:59]
	v_mfma_f32_16x16x128_f8f6f4 v[44:47], v[16:23], v[232:239], v[44:47]
	v_mfma_f32_16x16x128_f8f6f4 v[40:43], v[24:31], v[232:239], v[40:43]
	s_setprio 0
	s_setprio 1
	v_mfma_f32_16x16x128_f8f6f4 v[84:87], v[0:7], v[208:215], v[84:87]
	v_mfma_f32_16x16x128_f8f6f4 v[80:83], v[8:15], v[208:215], v[80:83]
	v_mfma_f32_16x16x128_f8f6f4 v[68:71], v[0:7], v[216:223], v[68:71]
	v_mfma_f32_16x16x128_f8f6f4 v[64:67], v[8:15], v[216:223], v[64:67]
	v_mfma_f32_16x16x128_f8f6f4 v[52:55], v[0:7], v[224:231], v[52:55]
	v_mfma_f32_16x16x128_f8f6f4 v[48:51], v[8:15], v[224:231], v[48:51]
	v_mfma_f32_16x16x128_f8f6f4 v[36:39], v[0:7], v[232:239], v[36:39]
	v_mfma_f32_16x16x128_f8f6f4 v[32:35], v[8:15], v[232:239], v[32:35]
	s_setprio 0
	s_barrier
	v_lshl_add_u64 v[240:241], s[42:43], 0, v[160:161]
	s_mov_b32 m0, s33
	s_nop 0
	global_load_lds_dwordx4 v[240:241], off
	v_lshl_add_u64 v[240:241], s[42:43], 0, v[164:165]
	s_mov_b32 m0, s48
	s_nop 0
	global_load_lds_dwordx4 v[240:241], off
	ds_read_b128 v[0:3], v197
	ds_read_b128 v[4:7], v198
	ds_read_b128 v[8:11], v199
	ds_read_b128 v[12:15], v200
	ds_read_b128 v[16:19], v201
	ds_read_b128 v[20:23], v202
	ds_read_b128 v[24:27], v203
	ds_read_b128 v[28:31], v204
	s_add_u32 s42, s42, 0x80000
	s_addc_u32 s43, s43, 0
	s_mov_b32 m0, s49
	v_lshl_add_u64 v[240:241], s[42:43], 0, v[160:161]
	ds_read_b128 v[208:211], v205 offset:32768
	ds_read_b128 v[212:215], v205 offset:33792
	ds_read_b128 v[216:219], v205 offset:34816
	ds_read_b128 v[220:223], v205 offset:35840
	ds_read_b128 v[224:227], v205 offset:36864
	ds_read_b128 v[228:231], v205 offset:37888
	ds_read_b128 v[232:235], v205 offset:38912
	ds_read_b128 v[236:239], v205 offset:39936
	global_load_lds_dwordx4 v[240:241], off
	v_lshl_add_u64 v[240:241], s[42:43], 0, v[164:165]
	s_mov_b32 m0, s50
	s_nop 0
	global_load_lds_dwordx4 v[240:241], off
	s_waitcnt vmcnt(8)
	s_waitcnt lgkmcnt(0)
	s_barrier
	s_setprio 1
	s_waitcnt lgkmcnt(0)
	v_mfma_f32_16x16x128_f8f6f4 v[156:159], v[0:7], v[208:215], v[156:159]
	v_mfma_f32_16x16x128_f8f6f4 v[152:155], v[8:15], v[208:215], v[152:155]
	v_mfma_f32_16x16x128_f8f6f4 v[140:143], v[0:7], v[216:223], v[140:143]
	v_mfma_f32_16x16x128_f8f6f4 v[136:139], v[8:15], v[216:223], v[136:139]
	v_mfma_f32_16x16x128_f8f6f4 v[124:127], v[0:7], v[224:231], v[124:127]
	v_mfma_f32_16x16x128_f8f6f4 v[120:123], v[8:15], v[224:231], v[120:123]
	v_mfma_f32_16x16x128_f8f6f4 v[108:111], v[0:7], v[232:239], v[108:111]
	v_mfma_f32_16x16x128_f8f6f4 v[104:107], v[8:15], v[232:239], v[104:107]
	s_setprio 0
	s_setprio 1
	v_mfma_f32_16x16x128_f8f6f4 v[148:151], v[16:23], v[208:215], v[148:151]
	v_mfma_f32_16x16x128_f8f6f4 v[144:147], v[24:31], v[208:215], v[144:147]
	v_mfma_f32_16x16x128_f8f6f4 v[132:135], v[16:23], v[216:223], v[132:135]
	v_mfma_f32_16x16x128_f8f6f4 v[128:131], v[24:31], v[216:223], v[128:131]
	v_mfma_f32_16x16x128_f8f6f4 v[116:119], v[16:23], v[224:231], v[116:119]
	v_mfma_f32_16x16x128_f8f6f4 v[112:115], v[24:31], v[224:231], v[112:115]
	v_mfma_f32_16x16x128_f8f6f4 v[100:103], v[16:23], v[232:239], v[100:103]
	v_mfma_f32_16x16x128_f8f6f4 v[96:99], v[24:31], v[232:239], v[96:99]
	s_setprio 0
	s_barrier
	s_mov_b32 m0, s51
	v_lshl_add_u64 v[180:181], v[180:181], 0, s[12:13]
	s_add_u32 s40, s40, 0x80080
	ds_read_b128 v[208:211], v205 offset:49152
	ds_read_b128 v[212:215], v205 offset:50176
	ds_read_b128 v[216:219], v205 offset:51200
	ds_read_b128 v[220:223], v205 offset:52224
	ds_read_b128 v[224:227], v205 offset:53248
	ds_read_b128 v[228:231], v205 offset:54272
	ds_read_b128 v[232:235], v205 offset:55296
	ds_read_b128 v[236:239], v205 offset:56320
	global_load_lds_dwordx4 v[180:181], off
	v_lshl_add_u64 v[180:181], v[182:183], 0, s[12:13]
	s_mov_b32 m0, s52
	s_addc_u32 s41, s41, 0
	global_load_lds_dwordx4 v[180:181], off
	v_lshl_add_u64 v[180:181], s[40:41], 0, v[162:163]
	s_mov_b32 m0, s55
	s_nop 0
	global_load_lds_dwordx4 v[180:181], off
	v_lshl_add_u64 v[180:181], s[40:41], 0, v[166:167]
	s_mov_b32 m0, s56
	s_nop 0
	global_load_lds_dwordx4 v[180:181], off
	s_waitcnt vmcnt(6)
	s_waitcnt lgkmcnt(0)
	s_barrier
	s_setprio 1
	s_waitcnt lgkmcnt(0)
	v_mfma_f32_16x16x128_f8f6f4 v[92:95], v[0:7], v[208:215], v[92:95]
	v_mfma_f32_16x16x128_f8f6f4 v[88:91], v[8:15], v[208:215], v[88:91]
	v_mfma_f32_16x16x128_f8f6f4 v[76:79], v[0:7], v[216:223], v[76:79]
	v_mfma_f32_16x16x128_f8f6f4 v[72:75], v[8:15], v[216:223], v[72:75]
	v_mfma_f32_16x16x128_f8f6f4 v[60:63], v[0:7], v[224:231], v[60:63]
	v_mfma_f32_16x16x128_f8f6f4 v[56:59], v[8:15], v[224:231], v[56:59]
	v_mfma_f32_16x16x128_f8f6f4 v[44:47], v[0:7], v[232:239], v[44:47]
	v_mfma_f32_16x16x128_f8f6f4 v[40:43], v[8:15], v[232:239], v[40:43]
	s_setprio 0
	s_setprio 1
	v_mfma_f32_16x16x128_f8f6f4 v[84:87], v[16:23], v[208:215], v[84:87]
	v_mfma_f32_16x16x128_f8f6f4 v[80:83], v[24:31], v[208:215], v[80:83]
	v_mfma_f32_16x16x128_f8f6f4 v[68:71], v[16:23], v[216:223], v[68:71]
	v_mfma_f32_16x16x128_f8f6f4 v[64:67], v[24:31], v[216:223], v[64:67]
	v_mfma_f32_16x16x128_f8f6f4 v[52:55], v[16:23], v[224:231], v[52:55]
	v_mfma_f32_16x16x128_f8f6f4 v[48:51], v[24:31], v[224:231], v[48:51]
	v_mfma_f32_16x16x128_f8f6f4 v[36:39], v[16:23], v[232:239], v[36:39]
	v_mfma_f32_16x16x128_f8f6f4 v[32:35], v[24:31], v[232:239], v[32:35]
	s_setprio 0
	s_barrier
	s_add_i32 s64, s64, 2
	s_add_u32 s38, s38, 0x100
	s_addc_u32 s39, s39, 0
	s_add_u32 s60, s60, 0x100
	s_addc_u32 s61, s61, 0
	s_cmp_gt_u32 s64, 29
	s_cbranch_scc0 .LBB0_940
	s_nop 15
	s_nop 15
	s_and_b64 vcc, exec, s[14:15]
	s_cbranch_vccz .LBB0_943
	s_barrier

.LBB0_1358:
	s_add_u32 s30, s26, 0x1000
	s_addc_u32 s31, s27, 0
	v_lshl_add_u64 v[200:201], s[30:31], 0, v[160:161]
	s_mov_b32 m0, s49
	s_nop 0
	global_load_lds_dwordx4 v[200:201], off
	v_lshl_add_u64 v[200:201], s[30:31], 0, v[164:165]
	s_mov_b32 m0, s50
	s_nop 0
	global_load_lds_dwordx4 v[200:201], off
	ds_read_b128 v[16:19], v207
	ds_read_b128 v[20:23], v208
	ds_read_b128 v[24:27], v209
	ds_read_b128 v[28:31], v210
	ds_read_b128 v[0:3], v211
	ds_read_b128 v[4:7], v212
	ds_read_b128 v[8:11], v213
	ds_read_b128 v[12:15], v214
	s_add_u32 s28, s26, 0x10000
	s_addc_u32 s29, s27, 0
	s_cmpk_eq_i32 s59, 0x7c
	s_cselect_b32 s36, s55, s28
	s_cselect_b32 s37, s19, s29
	s_cselect_b32 s34, s56, s57
	s_cselect_b32 s35, s17, s58
	v_lshl_add_u64 v[200:201], s[26:27], 0, v[168:169]
	s_add_i32 m0, s25, 0xc000
	ds_read_b128 v[176:179], v224
	ds_read_b128 v[180:183], v224 offset:1024
	ds_read_b128 v[184:187], v224 offset:2048
	ds_read_b128 v[188:191], v224 offset:3072
	ds_read_b128 v[192:195], v224 offset:4096
	ds_read_b128 v[196:199], v224 offset:5120
	ds_read_b128 v[226:229], v224 offset:6144
	ds_read_b128 v[230:233], v224 offset:7168
	global_load_lds_dwordx4 v[200:201], off
	v_lshl_add_u64 v[200:201], s[26:27], 0, v[170:171]
	s_add_i32 m0, s25, 0xe000
	s_nop 0
	global_load_lds_dwordx4 v[200:201], off
	s_waitcnt vmcnt(8)
	s_waitcnt lgkmcnt(0)
	s_barrier
	s_setprio 1
	s_waitcnt lgkmcnt(0)
	v_mfma_f32_16x16x128_f8f6f4 v[156:159], v[16:23], v[176:183], v[156:159]
	v_mfma_f32_16x16x128_f8f6f4 v[152:155], v[24:31], v[176:183], v[152:155]
	v_mfma_f32_16x16x128_f8f6f4 v[144:147], v[16:23], v[184:191], v[144:147]
	v_mfma_f32_16x16x128_f8f6f4 v[136:139], v[24:31], v[184:191], v[136:139]
	v_mfma_f32_16x16x128_f8f6f4 v[124:127], v[16:23], v[192:199], v[124:127]
	v_mfma_f32_16x16x128_f8f6f4 v[120:123], v[24:31], v[192:199], v[120:123]
	v_mfma_f32_16x16x128_f8f6f4 v[112:115], v[16:23], v[226:233], v[112:115]
	v_mfma_f32_16x16x128_f8f6f4 v[104:107], v[24:31], v[226:233], v[104:107]
	s_setprio 0
	s_setprio 1
	v_mfma_f32_16x16x128_f8f6f4 v[148:151], v[0:7], v[176:183], v[148:151]
	v_mfma_f32_16x16x128_f8f6f4 v[140:143], v[8:15], v[176:183], v[140:143]
	v_mfma_f32_16x16x128_f8f6f4 v[132:135], v[0:7], v[184:191], v[132:135]
	v_mfma_f32_16x16x128_f8f6f4 v[128:131], v[8:15], v[184:191], v[128:131]
	v_mfma_f32_16x16x128_f8f6f4 v[116:119], v[0:7], v[192:199], v[116:119]
	v_mfma_f32_16x16x128_f8f6f4 v[108:111], v[8:15], v[192:199], v[108:111]
	v_mfma_f32_16x16x128_f8f6f4 v[100:103], v[0:7], v[226:233], v[100:103]
	v_mfma_f32_16x16x128_f8f6f4 v[96:99], v[8:15], v[226:233], v[96:99]
	s_setprio 0
	s_barrier
	s_mov_b32 m0, s33
	v_lshl_add_u64 v[176:177], s[34:35], 0, v[162:163]
	s_add_u32 s26, s34, 0x200000
	ds_read_b128 v[180:183], v224 offset:16384
	ds_read_b128 v[184:187], v224 offset:17408
	ds_read_b128 v[188:191], v224 offset:18432
	ds_read_b128 v[192:195], v224 offset:19456
	ds_read_b128 v[196:199], v224 offset:20480
	ds_read_b128 v[200:203], v224 offset:21504
	ds_read_b128 v[226:229], v224 offset:22528
	ds_read_b128 v[230:233], v224 offset:23552
	global_load_lds_dwordx4 v[176:177], off
	v_lshl_add_u64 v[178:179], s[34:35], 0, v[166:167]
	s_mov_b32 m0, s38
	s_addc_u32 s27, s35, 0
	global_load_lds_dwordx4 v[178:179], off
	v_lshl_add_u64 v[204:205], s[26:27], 0, v[162:163]
	s_mov_b32 m0, s39
	s_nop 0
	global_load_lds_dwordx4 v[204:205], off
	v_lshl_add_u64 v[204:205], s[26:27], 0, v[166:167]
	s_mov_b32 m0, s40
	s_nop 0
	global_load_lds_dwordx4 v[204:205], off
	s_waitcnt vmcnt(6)
	s_waitcnt lgkmcnt(0)
	s_barrier
	s_setprio 1
	s_waitcnt lgkmcnt(0)
	v_mfma_f32_16x16x128_f8f6f4 v[92:95], v[16:23], v[180:187], v[92:95]
	v_mfma_f32_16x16x128_f8f6f4 v[88:91], v[24:31], v[180:187], v[88:91]
	v_mfma_f32_16x16x128_f8f6f4 v[80:83], v[16:23], v[188:195], v[80:83]
	v_mfma_f32_16x16x128_f8f6f4 v[72:75], v[24:31], v[188:195], v[72:75]
	v_mfma_f32_16x16x128_f8f6f4 v[64:67], v[16:23], v[196:203], v[64:67]
	v_mfma_f32_16x16x128_f8f6f4 v[56:59], v[24:31], v[196:203], v[56:59]
	v_mfma_f32_16x16x128_f8f6f4 v[48:51], v[16:23], v[226:233], v[48:51]
	v_mfma_f32_16x16x128_f8f6f4 v[40:43], v[24:31], v[226:233], v[40:43]
	s_setprio 0
	s_setprio 1
	v_mfma_f32_16x16x128_f8f6f4 v[84:87], v[0:7], v[180:187], v[84:87]
	v_mfma_f32_16x16x128_f8f6f4 v[76:79], v[8:15], v[180:187], v[76:79]
	v_mfma_f32_16x16x128_f8f6f4 v[68:71], v[0:7], v[188:195], v[68:71]
	v_mfma_f32_16x16x128_f8f6f4 v[60:63], v[8:15], v[188:195], v[60:63]
	v_mfma_f32_16x16x128_f8f6f4 v[52:55], v[0:7], v[196:203], v[52:55]
	v_mfma_f32_16x16x128_f8f6f4 v[44:47], v[8:15], v[196:203], v[44:47]
	v_mfma_f32_16x16x128_f8f6f4 v[36:39], v[0:7], v[226:233], v[36:39]
	v_mfma_f32_16x16x128_f8f6f4 v[32:35], v[8:15], v[226:233], v[32:35]
	s_setprio 0
	s_barrier
	v_lshl_add_u64 v[204:205], s[36:37], 0, v[160:161]
	s_mov_b32 m0, s25
	s_nop 0
	global_load_lds_dwordx4 v[204:205], off
	v_lshl_add_u64 v[204:205], s[36:37], 0, v[164:165]
	s_mov_b32 m0, s41
	s_nop 0
	global_load_lds_dwordx4 v[204:205], off
	ds_read_b128 v[0:3], v215
	ds_read_b128 v[4:7], v216
	ds_read_b128 v[8:11], v217
	ds_read_b128 v[12:15], v218
	ds_read_b128 v[16:19], v219
	ds_read_b128 v[20:23], v220
	ds_read_b128 v[24:27], v221
	ds_read_b128 v[28:31], v222
	s_add_u32 s26, s36, 0x8000
	s_addc_u32 s27, s37, 0
	s_mov_b32 m0, s42
	v_lshl_add_u64 v[204:205], s[26:27], 0, v[160:161]
	ds_read_b128 v[180:183], v224 offset:32768
	ds_read_b128 v[184:187], v224 offset:33792
	ds_read_b128 v[188:191], v224 offset:34816
	ds_read_b128 v[192:195], v224 offset:35840
	ds_read_b128 v[196:199], v224 offset:36864
	ds_read_b128 v[200:203], v224 offset:37888
	ds_read_b128 v[226:229], v224 offset:38912
	ds_read_b128 v[230:233], v224 offset:39936
	global_load_lds_dwordx4 v[204:205], off
	v_lshl_add_u64 v[204:205], s[26:27], 0, v[164:165]
	s_mov_b32 m0, s43
	s_nop 0
	global_load_lds_dwordx4 v[204:205], off
	s_waitcnt vmcnt(8)
	s_waitcnt lgkmcnt(0)
	s_barrier
	s_setprio 1
	s_waitcnt lgkmcnt(0)
	v_mfma_f32_16x16x128_f8f6f4 v[156:159], v[0:7], v[180:187], v[156:159]
	v_mfma_f32_16x16x128_f8f6f4 v[152:155], v[8:15], v[180:187], v[152:155]
	v_mfma_f32_16x16x128_f8f6f4 v[144:147], v[0:7], v[188:195], v[144:147]
	v_mfma_f32_16x16x128_f8f6f4 v[136:139], v[8:15], v[188:195], v[136:139]
	v_mfma_f32_16x16x128_f8f6f4 v[124:127], v[0:7], v[196:203], v[124:127]
	v_mfma_f32_16x16x128_f8f6f4 v[120:123], v[8:15], v[196:203], v[120:123]
	v_mfma_f32_16x16x128_f8f6f4 v[112:115], v[0:7], v[226:233], v[112:115]
	v_mfma_f32_16x16x128_f8f6f4 v[104:107], v[8:15], v[226:233], v[104:107]
	s_setprio 0
	s_setprio 1
	v_mfma_f32_16x16x128_f8f6f4 v[148:151], v[16:23], v[180:187], v[148:151]
	v_mfma_f32_16x16x128_f8f6f4 v[140:143], v[24:31], v[180:187], v[140:143]
	v_mfma_f32_16x16x128_f8f6f4 v[132:135], v[16:23], v[188:195], v[132:135]
	v_mfma_f32_16x16x128_f8f6f4 v[128:131], v[24:31], v[188:195], v[128:131]
	v_mfma_f32_16x16x128_f8f6f4 v[116:119], v[16:23], v[196:203], v[116:119]
	v_mfma_f32_16x16x128_f8f6f4 v[108:111], v[24:31], v[196:203], v[108:111]
	v_mfma_f32_16x16x128_f8f6f4 v[100:103], v[16:23], v[226:233], v[100:103]
	v_mfma_f32_16x16x128_f8f6f4 v[96:99], v[24:31], v[226:233], v[96:99]
	s_setprio 0
	s_barrier
	s_mov_b32 m0, s47
	v_lshl_add_u64 v[176:177], v[176:177], 0, s[10:11]
	s_add_u32 s26, s34, 0x200080
	ds_read_b128 v[180:183], v224 offset:49152
	ds_read_b128 v[184:187], v224 offset:50176
	ds_read_b128 v[188:191], v224 offset:51200
	ds_read_b128 v[192:195], v224 offset:52224
	ds_read_b128 v[196:199], v224 offset:53248
	ds_read_b128 v[200:203], v224 offset:54272
	ds_read_b128 v[226:229], v224 offset:55296
	ds_read_b128 v[230:233], v224 offset:56320
	global_load_lds_dwordx4 v[176:177], off
	v_lshl_add_u64 v[176:177], v[178:179], 0, s[10:11]
	s_mov_b32 m0, s48
	s_addc_u32 s27, s35, 0
	global_load_lds_dwordx4 v[176:177], off
	v_lshl_add_u64 v[176:177], s[26:27], 0, v[162:163]
	s_mov_b32 m0, s51
	s_nop 0
	global_load_lds_dwordx4 v[176:177], off
	v_lshl_add_u64 v[176:177], s[26:27], 0, v[166:167]
	s_mov_b32 m0, s52
	s_nop 0
	global_load_lds_dwordx4 v[176:177], off
	s_waitcnt vmcnt(6)
	s_waitcnt lgkmcnt(0)
	s_barrier
	s_setprio 1
	s_waitcnt lgkmcnt(0)
	v_mfma_f32_16x16x128_f8f6f4 v[92:95], v[0:7], v[180:187], v[92:95]
	v_mfma_f32_16x16x128_f8f6f4 v[88:91], v[8:15], v[180:187], v[88:91]
	v_mfma_f32_16x16x128_f8f6f4 v[80:83], v[0:7], v[188:195], v[80:83]
	v_mfma_f32_16x16x128_f8f6f4 v[72:75], v[8:15], v[188:195], v[72:75]
	v_mfma_f32_16x16x128_f8f6f4 v[64:67], v[0:7], v[196:203], v[64:67]
	v_mfma_f32_16x16x128_f8f6f4 v[56:59], v[8:15], v[196:203], v[56:59]
	v_mfma_f32_16x16x128_f8f6f4 v[48:51], v[0:7], v[226:233], v[48:51]
	v_mfma_f32_16x16x128_f8f6f4 v[40:43], v[8:15], v[226:233], v[40:43]
	s_setprio 0
	s_setprio 1
	v_mfma_f32_16x16x128_f8f6f4 v[84:87], v[16:23], v[180:187], v[84:87]
	v_mfma_f32_16x16x128_f8f6f4 v[76:79], v[24:31], v[180:187], v[76:79]
	v_mfma_f32_16x16x128_f8f6f4 v[68:71], v[16:23], v[188:195], v[68:71]
	v_mfma_f32_16x16x128_f8f6f4 v[60:63], v[24:31], v[188:195], v[60:63]
	v_mfma_f32_16x16x128_f8f6f4 v[52:55], v[16:23], v[196:203], v[52:55]
	v_mfma_f32_16x16x128_f8f6f4 v[44:47], v[24:31], v[196:203], v[44:47]
	v_mfma_f32_16x16x128_f8f6f4 v[36:39], v[16:23], v[226:233], v[36:39]
	v_mfma_f32_16x16x128_f8f6f4 v[32:35], v[24:31], v[226:233], v[32:35]
	s_setprio 0
	s_barrier
	s_add_i32 s59, s59, 2
	s_add_u32 s57, s57, 0x100
	s_addc_u32 s58, s58, 0
	s_cmpk_gt_u32 s59, 0x7d
	s_mov_b64 s[26:27], s[28:29]
	s_cbranch_scc0 .LBB0_1358
	s_nop 15
	s_nop 15
	s_and_b64 vcc, exec, s[12:13]
	s_cbranch_vccz .LBB0_1361
	s_barrier
